# combined bundle: v41 + sb wave remap + P7 epilogue 32-bit offsets/zero-init removal + P6 x16 fold into up-MFMA block scale
# speedup vs baseline: 1.0034x; 1.0022x over previous
; __device__ __forceinline__ unsigned pk4_fp8(float a, float b, float c, float d) { int r = __builtin_amdgcn_cvt_pk_fp8_f32(a, b, 0, false); r = __builtin_amdgcn_cvt_pk_fp8_f32(c, d, r, true); return (unsigned)r; }
;     __device__ __forceinline__ void operator()(const f32x4 (&acc)[2][2][4][2], const Unit& u, int wr, int wc, int fr, int fq) const {
;         const int row0 = u.pm * BM + wr * 64 + fr, col0 = (u.pn & 3) * 128 + wc * 32 + 8 * fq;
; #pragma unroll
;         for (int ai = 0; ai < 2; ++ai)
; #pragma unroll
;             for (int m = 0; m < 4; ++m) { float r[8];
; #pragma unroll
;                 for (int n = 0; n < 2; ++n)
; #pragma unroll
;                     for (int e = 0; e < 4; ++e) { const float g = acc[ai][0][m][n][e], up = acc[ai][1][m][n][e]; r[4 * n + e] = g * __builtin_amdgcn_rcpf(1.0f + __builtin_amdgcn_exp2f(-g * LOG2E)) * up * (float)(1 << ASHIFT); }
;                 v2u w; w.x = pk4_fp8(r[0], r[1], r[2], r[3]); w.y = pk4_fp8(r[4], r[5], r[6], r[7]);
;                 *(v2u*)(O + (size_t)(row0 + ai * HALF + m * 16) * EH + col0) = w; }
;     }
.LBB0_751:
	s_mov_b32 s98, 0xbfb8aa3b
	s_nop 15
	s_nop 15
	v_lshl_add_u32 v4, s88, 8, v203
	s_lshl_b32 s6, s89, 7
	s_and_b32 s6, s6, 0x180
	v_ashrrev_i32_e32 v5, 31, v4
	v_add_u32_e32 v2, s6, v205
	v_lshlrev_b64 v[0:1], 9, v[4:5]
	v_ashrrev_i32_e32 v3, 31, v2
	v_lshl_add_u64 v[0:1], s[24:25], 0, v[0:1]
	v_lshl_add_u64 v[0:1], v[0:1], 0, v[2:3]
	v_pk_mul_f32 v[228:229], v[192:193], s[98:99] op_sel_hi:[1,0]
	v_pk_mul_f32 v[230:231], v[194:195], s[98:99] op_sel_hi:[1,0]
	v_pk_mul_f32 v[232:233], v[184:185], s[98:99] op_sel_hi:[1,0]
	v_pk_mul_f32 v[234:235], v[186:187], s[98:99] op_sel_hi:[1,0]
	v_exp_f32_e32 v228, v228
	v_exp_f32_e32 v229, v229
	v_exp_f32_e32 v230, v230
	v_exp_f32_e32 v231, v231
	v_exp_f32_e32 v232, v232
	v_exp_f32_e32 v233, v233
	v_exp_f32_e32 v234, v234
	v_exp_f32_e32 v235, v235
	v_pk_add_f32 v[228:229], v[228:229], 1.0 op_sel_hi:[1,0]
	v_pk_add_f32 v[230:231], v[230:231], 1.0 op_sel_hi:[1,0]
	v_pk_add_f32 v[232:233], v[232:233], 1.0 op_sel_hi:[1,0]
	v_pk_add_f32 v[234:235], v[234:235], 1.0 op_sel_hi:[1,0]
	v_rcp_f32_e32 v228, v228
	v_rcp_f32_e32 v229, v229
	v_rcp_f32_e32 v230, v230
	v_rcp_f32_e32 v231, v231
	v_rcp_f32_e32 v232, v232
	v_rcp_f32_e32 v233, v233
	v_rcp_f32_e32 v234, v234
	v_rcp_f32_e32 v235, v235
	v_pk_mul_f32 v[228:229], v[192:193], v[228:229]
	v_pk_mul_f32 v[230:231], v[194:195], v[230:231]
	v_pk_mul_f32 v[232:233], v[184:185], v[232:233]
	v_pk_mul_f32 v[234:235], v[186:187], v[234:235]
	v_pk_mul_f32 v[228:229], v[188:189], v[228:229]
	v_pk_mul_f32 v[230:231], v[190:191], v[230:231]
	v_pk_mul_f32 v[232:233], v[180:181], v[232:233]
	v_pk_mul_f32 v[234:235], v[182:183], v[234:235]
	v_cvt_pk_fp8_f32 v244, v228, v229
	v_cvt_pk_fp8_f32 v245, v232, v233
	v_cvt_pk_fp8_f32 v244, v230, v231 op_sel:[0,0,1]
	v_cvt_pk_fp8_f32 v245, v234, v235 op_sel:[0,0,1]
	s_nop 0
	global_store_dwordx2 v[0:1], v[244:245], off
	v_or_b32_e32 v8, 16, v4
	v_ashrrev_i32_e32 v9, 31, v8
	v_lshlrev_b64 v[8:9], 9, v[8:9]
	v_lshl_add_u64 v[8:9], s[24:25], 0, v[8:9]
	v_lshl_add_u64 v[8:9], v[8:9], 0, v[2:3]
	v_pk_mul_f32 v[228:229], v[176:177], s[98:99] op_sel_hi:[1,0]
	v_pk_mul_f32 v[230:231], v[178:179], s[98:99] op_sel_hi:[1,0]
	v_pk_mul_f32 v[232:233], v[168:169], s[98:99] op_sel_hi:[1,0]
	v_pk_mul_f32 v[234:235], v[170:171], s[98:99] op_sel_hi:[1,0]
	v_exp_f32_e32 v228, v228
	v_exp_f32_e32 v229, v229
	v_exp_f32_e32 v230, v230
	v_exp_f32_e32 v231, v231
	v_exp_f32_e32 v232, v232
	v_exp_f32_e32 v233, v233
	v_exp_f32_e32 v234, v234
	v_exp_f32_e32 v235, v235
	v_pk_add_f32 v[228:229], v[228:229], 1.0 op_sel_hi:[1,0]
	v_pk_add_f32 v[230:231], v[230:231], 1.0 op_sel_hi:[1,0]
	v_pk_add_f32 v[232:233], v[232:233], 1.0 op_sel_hi:[1,0]
	v_pk_add_f32 v[234:235], v[234:235], 1.0 op_sel_hi:[1,0]
	v_rcp_f32_e32 v228, v228
	v_rcp_f32_e32 v229, v229
	v_rcp_f32_e32 v230, v230
	v_rcp_f32_e32 v231, v231
	v_rcp_f32_e32 v232, v232
	v_rcp_f32_e32 v233, v233
	v_rcp_f32_e32 v234, v234
	v_rcp_f32_e32 v235, v235
	v_pk_mul_f32 v[228:229], v[176:177], v[228:229]
	v_pk_mul_f32 v[230:231], v[178:179], v[230:231]
	v_pk_mul_f32 v[232:233], v[168:169], v[232:233]
	v_pk_mul_f32 v[234:235], v[170:171], v[234:235]
	v_pk_mul_f32 v[228:229], v[172:173], v[228:229]
	v_pk_mul_f32 v[230:231], v[174:175], v[230:231]
	v_pk_mul_f32 v[232:233], v[164:165], v[232:233]
	v_pk_mul_f32 v[234:235], v[166:167], v[234:235]
	v_cvt_pk_fp8_f32 v244, v228, v229
	v_cvt_pk_fp8_f32 v245, v232, v233
	v_cvt_pk_fp8_f32 v244, v230, v231 op_sel:[0,0,1]
	v_cvt_pk_fp8_f32 v245, v234, v235 op_sel:[0,0,1]
	s_nop 0
	global_store_dwordx2 v[8:9], v[244:245], off
	v_or_b32_e32 v8, 32, v4
	v_ashrrev_i32_e32 v9, 31, v8
	v_lshlrev_b64 v[8:9], 9, v[8:9]
	v_lshl_add_u64 v[8:9], s[24:25], 0, v[8:9]
	v_lshl_add_u64 v[8:9], v[8:9], 0, v[2:3]
	v_pk_mul_f32 v[228:229], v[160:161], s[98:99] op_sel_hi:[1,0]
	v_pk_mul_f32 v[230:231], v[162:163], s[98:99] op_sel_hi:[1,0]
	v_pk_mul_f32 v[232:233], v[152:153], s[98:99] op_sel_hi:[1,0]
	v_pk_mul_f32 v[234:235], v[154:155], s[98:99] op_sel_hi:[1,0]
	v_exp_f32_e32 v228, v228
	v_exp_f32_e32 v229, v229
	v_exp_f32_e32 v230, v230
	v_exp_f32_e32 v231, v231
	v_exp_f32_e32 v232, v232
	v_exp_f32_e32 v233, v233
	v_exp_f32_e32 v234, v234
	v_exp_f32_e32 v235, v235
	v_pk_add_f32 v[228:229], v[228:229], 1.0 op_sel_hi:[1,0]
	v_pk_add_f32 v[230:231], v[230:231], 1.0 op_sel_hi:[1,0]
	v_pk_add_f32 v[232:233], v[232:233], 1.0 op_sel_hi:[1,0]
	v_pk_add_f32 v[234:235], v[234:235], 1.0 op_sel_hi:[1,0]
	v_rcp_f32_e32 v228, v228
	v_rcp_f32_e32 v229, v229
	v_rcp_f32_e32 v230, v230
	v_rcp_f32_e32 v231, v231
	v_rcp_f32_e32 v232, v232
	v_rcp_f32_e32 v233, v233
	v_rcp_f32_e32 v234, v234
	v_rcp_f32_e32 v235, v235
	v_pk_mul_f32 v[228:229], v[160:161], v[228:229]
	v_pk_mul_f32 v[230:231], v[162:163], v[230:231]
	v_pk_mul_f32 v[232:233], v[152:153], v[232:233]
	v_pk_mul_f32 v[234:235], v[154:155], v[234:235]
	v_pk_mul_f32 v[228:229], v[156:157], v[228:229]
	v_pk_mul_f32 v[230:231], v[158:159], v[230:231]
	v_pk_mul_f32 v[232:233], v[148:149], v[232:233]
	v_pk_mul_f32 v[234:235], v[150:151], v[234:235]
	v_cvt_pk_fp8_f32 v244, v228, v229
	v_cvt_pk_fp8_f32 v245, v232, v233
	v_cvt_pk_fp8_f32 v244, v230, v231 op_sel:[0,0,1]
	v_cvt_pk_fp8_f32 v245, v234, v235 op_sel:[0,0,1]
	s_nop 0
	global_store_dwordx2 v[8:9], v[244:245], off
	v_or_b32_e32 v4, 48, v4
	v_ashrrev_i32_e32 v5, 31, v4
	v_lshlrev_b64 v[4:5], 9, v[4:5]
	v_lshl_add_u64 v[4:5], s[24:25], 0, v[4:5]
	v_lshl_add_u64 v[2:3], v[4:5], 0, v[2:3]
	v_pk_mul_f32 v[228:229], v[144:145], s[98:99] op_sel_hi:[1,0]
	v_pk_mul_f32 v[230:231], v[146:147], s[98:99] op_sel_hi:[1,0]
	v_pk_mul_f32 v[232:233], v[136:137], s[98:99] op_sel_hi:[1,0]
	v_pk_mul_f32 v[234:235], v[138:139], s[98:99] op_sel_hi:[1,0]
; __device__ __forceinline__ unsigned pk4_fp8(float a, float b, float c, float d) { int r = __builtin_amdgcn_cvt_pk_fp8_f32(a, b, 0, false); r = __builtin_amdgcn_cvt_pk_fp8_f32(c, d, r, true); return (unsigned)r; }
;     __device__ __forceinline__ void operator()(const f32x4 (&acc)[2][2][4][2], const Unit& u, int wr, int wc, int fr, int fq) const {
;         const int row0 = u.pm * BM + wr * 64 + fr, col0 = (u.pn & 3) * 128 + wc * 32 + 8 * fq;
; #pragma unroll
;         for (int ai = 0; ai < 2; ++ai)
; #pragma unroll
;             for (int m = 0; m < 4; ++m) { float r[8];
; #pragma unroll
;                 for (int n = 0; n < 2; ++n)
; #pragma unroll
;                     for (int e = 0; e < 4; ++e) { const float g = acc[ai][0][m][n][e], up = acc[ai][1][m][n][e]; r[4 * n + e] = g * __builtin_amdgcn_rcpf(1.0f + __builtin_amdgcn_exp2f(-g * LOG2E)) * up * (float)(1 << ASHIFT); }
;                 v2u w; w.x = pk4_fp8(r[0], r[1], r[2], r[3]); w.y = pk4_fp8(r[4], r[5], r[6], r[7]);
;                 *(v2u*)(O + (size_t)(row0 + ai * HALF + m * 16) * EH + col0) = w; }
;     }
	v_exp_f32_e32 v228, v228
	v_exp_f32_e32 v229, v229
	v_exp_f32_e32 v230, v230
	v_exp_f32_e32 v231, v231
	v_exp_f32_e32 v232, v232
	v_exp_f32_e32 v233, v233
	v_exp_f32_e32 v234, v234
	v_exp_f32_e32 v235, v235
	v_pk_add_f32 v[228:229], v[228:229], 1.0 op_sel_hi:[1,0]
	v_pk_add_f32 v[230:231], v[230:231], 1.0 op_sel_hi:[1,0]
	v_pk_add_f32 v[232:233], v[232:233], 1.0 op_sel_hi:[1,0]
	v_pk_add_f32 v[234:235], v[234:235], 1.0 op_sel_hi:[1,0]
	v_rcp_f32_e32 v228, v228
	v_rcp_f32_e32 v229, v229
	v_rcp_f32_e32 v230, v230
	v_rcp_f32_e32 v231, v231
	v_rcp_f32_e32 v232, v232
	v_rcp_f32_e32 v233, v233
	v_rcp_f32_e32 v234, v234
	v_rcp_f32_e32 v235, v235
	v_pk_mul_f32 v[228:229], v[144:145], v[228:229]
	v_pk_mul_f32 v[230:231], v[146:147], v[230:231]
	v_pk_mul_f32 v[232:233], v[136:137], v[232:233]
	v_pk_mul_f32 v[234:235], v[138:139], v[234:235]
	v_pk_mul_f32 v[228:229], v[140:141], v[228:229]
	v_pk_mul_f32 v[230:231], v[142:143], v[230:231]
	v_pk_mul_f32 v[232:233], v[132:133], v[232:233]
	v_pk_mul_f32 v[234:235], v[134:135], v[234:235]
	v_cvt_pk_fp8_f32 v244, v228, v229
	v_cvt_pk_fp8_f32 v245, v232, v233
	v_cvt_pk_fp8_f32 v244, v230, v231 op_sel:[0,0,1]
	v_cvt_pk_fp8_f32 v245, v234, v235 op_sel:[0,0,1]
	s_nop 0
	global_store_dwordx2 v[2:3], v[244:245], off
	v_add_co_u32_e32 v4, vcc, s50, v0
	s_nop 0
	v_addc_co_u32_e32 v5, vcc, 0, v1, vcc
	v_pk_mul_f32 v[228:229], v[128:129], s[98:99] op_sel_hi:[1,0]
	v_pk_mul_f32 v[230:231], v[130:131], s[98:99] op_sel_hi:[1,0]
	v_pk_mul_f32 v[232:233], v[120:121], s[98:99] op_sel_hi:[1,0]
	v_pk_mul_f32 v[234:235], v[122:123], s[98:99] op_sel_hi:[1,0]
	v_exp_f32_e32 v228, v228
	v_exp_f32_e32 v229, v229
	v_exp_f32_e32 v230, v230
	v_exp_f32_e32 v231, v231
	v_exp_f32_e32 v232, v232
	v_exp_f32_e32 v233, v233
	v_exp_f32_e32 v234, v234
	v_exp_f32_e32 v235, v235
	v_pk_add_f32 v[228:229], v[228:229], 1.0 op_sel_hi:[1,0]
	v_pk_add_f32 v[230:231], v[230:231], 1.0 op_sel_hi:[1,0]
	v_pk_add_f32 v[232:233], v[232:233], 1.0 op_sel_hi:[1,0]
	v_pk_add_f32 v[234:235], v[234:235], 1.0 op_sel_hi:[1,0]
	v_rcp_f32_e32 v228, v228
	v_rcp_f32_e32 v229, v229
	v_rcp_f32_e32 v230, v230
	v_rcp_f32_e32 v231, v231
	v_rcp_f32_e32 v232, v232
	v_rcp_f32_e32 v233, v233
	v_rcp_f32_e32 v234, v234
	v_rcp_f32_e32 v235, v235
	v_pk_mul_f32 v[228:229], v[128:129], v[228:229]
	v_pk_mul_f32 v[230:231], v[130:131], v[230:231]
	v_pk_mul_f32 v[232:233], v[120:121], v[232:233]
	v_pk_mul_f32 v[234:235], v[122:123], v[234:235]
	v_pk_mul_f32 v[228:229], v[124:125], v[228:229]
	v_pk_mul_f32 v[230:231], v[126:127], v[230:231]
	v_pk_mul_f32 v[232:233], v[116:117], v[232:233]
	v_pk_mul_f32 v[234:235], v[118:119], v[234:235]
	v_cvt_pk_fp8_f32 v244, v228, v229
	v_cvt_pk_fp8_f32 v245, v232, v233
	v_cvt_pk_fp8_f32 v244, v230, v231 op_sel:[0,0,1]
	v_cvt_pk_fp8_f32 v245, v234, v235 op_sel:[0,0,1]
	s_nop 0
	global_store_dwordx2 v[4:5], v[244:245], off
	v_add_co_u32_e32 v4, vcc, s52, v0
	s_nop 0
	v_addc_co_u32_e32 v5, vcc, 0, v1, vcc
	v_pk_mul_f32 v[228:229], v[112:113], s[98:99] op_sel_hi:[1,0]
	v_pk_mul_f32 v[230:231], v[114:115], s[98:99] op_sel_hi:[1,0]
	v_pk_mul_f32 v[232:233], v[104:105], s[98:99] op_sel_hi:[1,0]
	v_pk_mul_f32 v[234:235], v[106:107], s[98:99] op_sel_hi:[1,0]
	v_exp_f32_e32 v228, v228
	v_exp_f32_e32 v229, v229
	v_exp_f32_e32 v230, v230
	v_exp_f32_e32 v231, v231
	v_exp_f32_e32 v232, v232
	v_exp_f32_e32 v233, v233
	v_exp_f32_e32 v234, v234
	v_exp_f32_e32 v235, v235
	v_pk_add_f32 v[228:229], v[228:229], 1.0 op_sel_hi:[1,0]
	v_pk_add_f32 v[230:231], v[230:231], 1.0 op_sel_hi:[1,0]
	v_pk_add_f32 v[232:233], v[232:233], 1.0 op_sel_hi:[1,0]
	v_pk_add_f32 v[234:235], v[234:235], 1.0 op_sel_hi:[1,0]
	v_rcp_f32_e32 v228, v228
	v_rcp_f32_e32 v229, v229
	v_rcp_f32_e32 v230, v230
	v_rcp_f32_e32 v231, v231
	v_rcp_f32_e32 v232, v232
	v_rcp_f32_e32 v233, v233
	v_rcp_f32_e32 v234, v234
	v_rcp_f32_e32 v235, v235
	v_pk_mul_f32 v[228:229], v[112:113], v[228:229]
; #define PG8_BAR __builtin_amdgcn_s_barrier()
; __device__ __forceinline__ unsigned pk4_fp8(float a, float b, float c, float d) { int r = __builtin_amdgcn_cvt_pk_fp8_f32(a, b, 0, false); r = __builtin_amdgcn_cvt_pk_fp8_f32(c, d, r, true); return (unsigned)r; }
; template <class Epi, class Sched, bool ALIGN_EPI, bool FP8 = false>
; __device__ __forceinline__ void gemm_phase(PG8_LAS unsigned char* lds, const Gemm g, const Sched& S, const Epi& E, const int wid, const int lane) {
;     ...
;         if (!has_next) break;
; #pragma unroll
;         for (int a = 0; a < 2; ++a)
; #pragma unroll
;             for (int b = 0; b < 2; ++b)
; #pragma unroll
;                 for (int m = 0; m < 4; ++m)
; #pragma unroll
;                     for (int n = 0; n < 2; ++n) acc[a][b][m][n] = (f32x4){0.f, 0.f, 0.f, 0.f};
;         cur = nxt; cA = nA; cB = nB; ++ui;
;         if constexpr (ALIGN_EPI) { if (wr == 1) PG8_BAR; }
;     __device__ __forceinline__ void operator()(const f32x4 (&acc)[2][2][4][2], const Unit& u, int wr, int wc, int fr, int fq) const {
;         const int row0 = u.pm * BM + wr * 64 + fr, col0 = (u.pn & 3) * 128 + wc * 32 + 8 * fq;
; #pragma unroll
;         for (int ai = 0; ai < 2; ++ai)
; #pragma unroll
;             for (int m = 0; m < 4; ++m) { float r[8];
; #pragma unroll
;                 for (int n = 0; n < 2; ++n)
; #pragma unroll
;                     for (int e = 0; e < 4; ++e) { const float g = acc[ai][0][m][n][e], up = acc[ai][1][m][n][e]; r[4 * n + e] = g * __builtin_amdgcn_rcpf(1.0f + __builtin_amdgcn_exp2f(-g * LOG2E)) * up * (float)(1 << ASHIFT); }
;                 v2u w; w.x = pk4_fp8(r[0], r[1], r[2], r[3]); w.y = pk4_fp8(r[4], r[5], r[6], r[7]);
;                 *(v2u*)(O + (size_t)(row0 + ai * HALF + m * 16) * EH + col0) = w; }
;     }
	v_pk_mul_f32 v[230:231], v[114:115], v[230:231]
	v_pk_mul_f32 v[232:233], v[104:105], v[232:233]
	v_pk_mul_f32 v[234:235], v[106:107], v[234:235]
	v_pk_mul_f32 v[228:229], v[108:109], v[228:229]
	v_pk_mul_f32 v[230:231], v[110:111], v[230:231]
	v_pk_mul_f32 v[232:233], v[100:101], v[232:233]
	v_pk_mul_f32 v[234:235], v[102:103], v[234:235]
	v_cvt_pk_fp8_f32 v244, v228, v229
	v_cvt_pk_fp8_f32 v245, v232, v233
	v_cvt_pk_fp8_f32 v244, v230, v231 op_sel:[0,0,1]
	v_cvt_pk_fp8_f32 v245, v234, v235 op_sel:[0,0,1]
	s_nop 0
	global_store_dwordx2 v[4:5], v[244:245], off
	v_add_co_u32_e32 v4, vcc, s54, v0
	s_nop 0
	v_addc_co_u32_e32 v5, vcc, 0, v1, vcc
	v_pk_mul_f32 v[228:229], v[96:97], s[98:99] op_sel_hi:[1,0]
	v_pk_mul_f32 v[230:231], v[98:99], s[98:99] op_sel_hi:[1,0]
	v_pk_mul_f32 v[232:233], v[88:89], s[98:99] op_sel_hi:[1,0]
	v_pk_mul_f32 v[234:235], v[90:91], s[98:99] op_sel_hi:[1,0]
	v_exp_f32_e32 v228, v228
	v_exp_f32_e32 v229, v229
	v_exp_f32_e32 v230, v230
	v_exp_f32_e32 v231, v231
	v_exp_f32_e32 v232, v232
	v_exp_f32_e32 v233, v233
	v_exp_f32_e32 v234, v234
	v_exp_f32_e32 v235, v235
	v_pk_add_f32 v[228:229], v[228:229], 1.0 op_sel_hi:[1,0]
	v_pk_add_f32 v[230:231], v[230:231], 1.0 op_sel_hi:[1,0]
	v_pk_add_f32 v[232:233], v[232:233], 1.0 op_sel_hi:[1,0]
	v_pk_add_f32 v[234:235], v[234:235], 1.0 op_sel_hi:[1,0]
	v_rcp_f32_e32 v228, v228
	v_rcp_f32_e32 v229, v229
	v_rcp_f32_e32 v230, v230
	v_rcp_f32_e32 v231, v231
	v_rcp_f32_e32 v232, v232
	v_rcp_f32_e32 v233, v233
	v_rcp_f32_e32 v234, v234
	v_rcp_f32_e32 v235, v235
	v_pk_mul_f32 v[228:229], v[96:97], v[228:229]
	v_pk_mul_f32 v[230:231], v[98:99], v[230:231]
	v_pk_mul_f32 v[232:233], v[88:89], v[232:233]
	v_pk_mul_f32 v[234:235], v[90:91], v[234:235]
	v_pk_mul_f32 v[228:229], v[92:93], v[228:229]
	v_pk_mul_f32 v[230:231], v[94:95], v[230:231]
	v_pk_mul_f32 v[232:233], v[84:85], v[232:233]
	v_pk_mul_f32 v[234:235], v[86:87], v[234:235]
	v_cvt_pk_fp8_f32 v244, v228, v229
	v_cvt_pk_fp8_f32 v245, v232, v233
	v_cvt_pk_fp8_f32 v244, v230, v231 op_sel:[0,0,1]
	v_cvt_pk_fp8_f32 v245, v234, v235 op_sel:[0,0,1]
	s_nop 0
	global_store_dwordx2 v[4:5], v[244:245], off
	v_add_co_u32_e32 v0, vcc, 0x16000, v0
	s_nop 1
	v_addc_co_u32_e32 v1, vcc, 0, v1, vcc
	s_and_b64 vcc, exec, s[4:5]
	s_mov_b64 s[4:5], -1
	v_pk_mul_f32 v[228:229], v[80:81], s[98:99] op_sel_hi:[1,0]
	v_pk_mul_f32 v[230:231], v[82:83], s[98:99] op_sel_hi:[1,0]
	v_pk_mul_f32 v[232:233], v[72:73], s[98:99] op_sel_hi:[1,0]
	v_pk_mul_f32 v[234:235], v[74:75], s[98:99] op_sel_hi:[1,0]
	v_exp_f32_e32 v228, v228
	v_exp_f32_e32 v229, v229
	v_exp_f32_e32 v230, v230
	v_exp_f32_e32 v231, v231
	v_exp_f32_e32 v232, v232
	v_exp_f32_e32 v233, v233
	v_exp_f32_e32 v234, v234
	v_exp_f32_e32 v235, v235
	v_pk_add_f32 v[228:229], v[228:229], 1.0 op_sel_hi:[1,0]
	v_pk_add_f32 v[230:231], v[230:231], 1.0 op_sel_hi:[1,0]
	v_pk_add_f32 v[232:233], v[232:233], 1.0 op_sel_hi:[1,0]
	v_pk_add_f32 v[234:235], v[234:235], 1.0 op_sel_hi:[1,0]
	v_rcp_f32_e32 v228, v228
	v_rcp_f32_e32 v229, v229
	v_rcp_f32_e32 v230, v230
	v_rcp_f32_e32 v231, v231
	v_rcp_f32_e32 v232, v232
	v_rcp_f32_e32 v233, v233
	v_rcp_f32_e32 v234, v234
	v_rcp_f32_e32 v235, v235
	v_pk_mul_f32 v[228:229], v[80:81], v[228:229]
	v_pk_mul_f32 v[230:231], v[82:83], v[230:231]
	v_pk_mul_f32 v[232:233], v[72:73], v[232:233]
	v_pk_mul_f32 v[234:235], v[74:75], v[234:235]
	v_pk_mul_f32 v[228:229], v[76:77], v[228:229]
	v_pk_mul_f32 v[230:231], v[78:79], v[230:231]
	v_pk_mul_f32 v[232:233], v[68:69], v[232:233]
	v_pk_mul_f32 v[234:235], v[70:71], v[234:235]
	v_cvt_pk_fp8_f32 v244, v228, v229
	v_cvt_pk_fp8_f32 v245, v232, v233
	v_cvt_pk_fp8_f32 v244, v230, v231 op_sel:[0,0,1]
	v_cvt_pk_fp8_f32 v245, v234, v235 op_sel:[0,0,1]
	s_nop 0
	global_store_dwordx2 v[0:1], v[244:245], off
	s_cbranch_vccnz .LBB0_715
	s_andn2_b64 vcc, exec, s[22:23]
	s_cbranch_vccnz .LBB0_714
	s_barrier
	s_branch .LBB0_714

; __device__ __forceinline__ unsigned pk4_fp8(float a, float b, float c, float d) { int r = __builtin_amdgcn_cvt_pk_fp8_f32(a, b, 0, false); r = __builtin_amdgcn_cvt_pk_fp8_f32(c, d, r, true); return (unsigned)r; }
;     __device__ __forceinline__ void operator()(const f32x4 (&acc)[2][2][4][2], const Unit& u, int wr, int wc, int fr, int fq) const {
;         const int row0 = u.pm * BM + wr * 64 + fr, col0 = (u.pn & 3) * 128 + wc * 32 + 8 * fq;
; #pragma unroll
;         for (int ai = 0; ai < 2; ++ai)
; #pragma unroll
;             for (int m = 0; m < 4; ++m) { float r[8];
; #pragma unroll
;                 for (int n = 0; n < 2; ++n)
; #pragma unroll
;                     for (int e = 0; e < 4; ++e) { const float g = acc[ai][0][m][n][e], up = acc[ai][1][m][n][e]; r[4 * n + e] = g * __builtin_amdgcn_rcpf(1.0f + __builtin_amdgcn_exp2f(-g * LOG2E)) * up * (float)(1 << ASHIFT); }
;                 v2u w; w.x = pk4_fp8(r[0], r[1], r[2], r[3]); w.y = pk4_fp8(r[4], r[5], r[6], r[7]);
;                 *(v2u*)(O + (size_t)(row0 + ai * HALF + m * 16) * EH + col0) = w; }
;     }
.LBB0_1661:
	s_mov_b32 s98, 0xbfb8aa3b
	s_nop 15
	s_nop 15
	v_lshl_add_u32 v4, s87, 8, v203
	s_lshl_b32 s6, s88, 7
	s_and_b32 s6, s6, 0x180
	v_ashrrev_i32_e32 v5, 31, v4
	v_add_u32_e32 v2, s6, v205
	v_lshlrev_b64 v[0:1], 9, v[4:5]
	v_ashrrev_i32_e32 v3, 31, v2
	v_lshl_add_u64 v[0:1], s[24:25], 0, v[0:1]
	v_lshl_add_u64 v[0:1], v[0:1], 0, v[2:3]
	v_pk_mul_f32 v[228:229], v[192:193], s[98:99] op_sel_hi:[1,0]
	v_pk_mul_f32 v[230:231], v[194:195], s[98:99] op_sel_hi:[1,0]
	v_pk_mul_f32 v[232:233], v[184:185], s[98:99] op_sel_hi:[1,0]
	v_pk_mul_f32 v[234:235], v[186:187], s[98:99] op_sel_hi:[1,0]
	v_exp_f32_e32 v228, v228
	v_exp_f32_e32 v229, v229
	v_exp_f32_e32 v230, v230
	v_exp_f32_e32 v231, v231
	v_exp_f32_e32 v232, v232
	v_exp_f32_e32 v233, v233
	v_exp_f32_e32 v234, v234
	v_exp_f32_e32 v235, v235
	v_pk_add_f32 v[228:229], v[228:229], 1.0 op_sel_hi:[1,0]
	v_pk_add_f32 v[230:231], v[230:231], 1.0 op_sel_hi:[1,0]
	v_pk_add_f32 v[232:233], v[232:233], 1.0 op_sel_hi:[1,0]
	v_pk_add_f32 v[234:235], v[234:235], 1.0 op_sel_hi:[1,0]
	v_rcp_f32_e32 v228, v228
	v_rcp_f32_e32 v229, v229
	v_rcp_f32_e32 v230, v230
	v_rcp_f32_e32 v231, v231
	v_rcp_f32_e32 v232, v232
	v_rcp_f32_e32 v233, v233
	v_rcp_f32_e32 v234, v234
	v_rcp_f32_e32 v235, v235
	v_pk_mul_f32 v[228:229], v[192:193], v[228:229]
	v_pk_mul_f32 v[230:231], v[194:195], v[230:231]
	v_pk_mul_f32 v[232:233], v[184:185], v[232:233]
	v_pk_mul_f32 v[234:235], v[186:187], v[234:235]
	v_pk_mul_f32 v[228:229], v[188:189], v[228:229]
	v_pk_mul_f32 v[230:231], v[190:191], v[230:231]
	v_pk_mul_f32 v[232:233], v[180:181], v[232:233]
	v_pk_mul_f32 v[234:235], v[182:183], v[234:235]
	v_cvt_pk_fp8_f32 v244, v228, v229
	v_cvt_pk_fp8_f32 v245, v232, v233
	v_cvt_pk_fp8_f32 v244, v230, v231 op_sel:[0,0,1]
	v_cvt_pk_fp8_f32 v245, v234, v235 op_sel:[0,0,1]
	s_nop 0
	global_store_dwordx2 v[0:1], v[244:245], off
	v_or_b32_e32 v8, 16, v4
	v_ashrrev_i32_e32 v9, 31, v8
	v_lshlrev_b64 v[8:9], 9, v[8:9]
	v_lshl_add_u64 v[8:9], s[24:25], 0, v[8:9]
	v_lshl_add_u64 v[8:9], v[8:9], 0, v[2:3]
	v_pk_mul_f32 v[228:229], v[176:177], s[98:99] op_sel_hi:[1,0]
	v_pk_mul_f32 v[230:231], v[178:179], s[98:99] op_sel_hi:[1,0]
	v_pk_mul_f32 v[232:233], v[168:169], s[98:99] op_sel_hi:[1,0]
	v_pk_mul_f32 v[234:235], v[170:171], s[98:99] op_sel_hi:[1,0]
	v_exp_f32_e32 v228, v228
	v_exp_f32_e32 v229, v229
	v_exp_f32_e32 v230, v230
	v_exp_f32_e32 v231, v231
	v_exp_f32_e32 v232, v232
	v_exp_f32_e32 v233, v233
	v_exp_f32_e32 v234, v234
	v_exp_f32_e32 v235, v235
	v_pk_add_f32 v[228:229], v[228:229], 1.0 op_sel_hi:[1,0]
	v_pk_add_f32 v[230:231], v[230:231], 1.0 op_sel_hi:[1,0]
	v_pk_add_f32 v[232:233], v[232:233], 1.0 op_sel_hi:[1,0]
	v_pk_add_f32 v[234:235], v[234:235], 1.0 op_sel_hi:[1,0]
	v_rcp_f32_e32 v228, v228
	v_rcp_f32_e32 v229, v229
	v_rcp_f32_e32 v230, v230
	v_rcp_f32_e32 v231, v231
	v_rcp_f32_e32 v232, v232
	v_rcp_f32_e32 v233, v233
	v_rcp_f32_e32 v234, v234
	v_rcp_f32_e32 v235, v235
	v_pk_mul_f32 v[228:229], v[176:177], v[228:229]
	v_pk_mul_f32 v[230:231], v[178:179], v[230:231]
	v_pk_mul_f32 v[232:233], v[168:169], v[232:233]
	v_pk_mul_f32 v[234:235], v[170:171], v[234:235]
	v_pk_mul_f32 v[228:229], v[172:173], v[228:229]
	v_pk_mul_f32 v[230:231], v[174:175], v[230:231]
	v_pk_mul_f32 v[232:233], v[164:165], v[232:233]
	v_pk_mul_f32 v[234:235], v[166:167], v[234:235]
	v_cvt_pk_fp8_f32 v244, v228, v229
	v_cvt_pk_fp8_f32 v245, v232, v233
	v_cvt_pk_fp8_f32 v244, v230, v231 op_sel:[0,0,1]
	v_cvt_pk_fp8_f32 v245, v234, v235 op_sel:[0,0,1]
	s_nop 0
	global_store_dwordx2 v[8:9], v[244:245], off
	v_or_b32_e32 v8, 32, v4
	v_ashrrev_i32_e32 v9, 31, v8
	v_lshlrev_b64 v[8:9], 9, v[8:9]
	v_lshl_add_u64 v[8:9], s[24:25], 0, v[8:9]
	v_lshl_add_u64 v[8:9], v[8:9], 0, v[2:3]
	v_pk_mul_f32 v[228:229], v[160:161], s[98:99] op_sel_hi:[1,0]
	v_pk_mul_f32 v[230:231], v[162:163], s[98:99] op_sel_hi:[1,0]
	v_pk_mul_f32 v[232:233], v[152:153], s[98:99] op_sel_hi:[1,0]
	v_pk_mul_f32 v[234:235], v[154:155], s[98:99] op_sel_hi:[1,0]
	v_exp_f32_e32 v228, v228
	v_exp_f32_e32 v229, v229
	v_exp_f32_e32 v230, v230
	v_exp_f32_e32 v231, v231
	v_exp_f32_e32 v232, v232
	v_exp_f32_e32 v233, v233
	v_exp_f32_e32 v234, v234
	v_exp_f32_e32 v235, v235
	v_pk_add_f32 v[228:229], v[228:229], 1.0 op_sel_hi:[1,0]
	v_pk_add_f32 v[230:231], v[230:231], 1.0 op_sel_hi:[1,0]
	v_pk_add_f32 v[232:233], v[232:233], 1.0 op_sel_hi:[1,0]
	v_pk_add_f32 v[234:235], v[234:235], 1.0 op_sel_hi:[1,0]
	v_rcp_f32_e32 v228, v228
	v_rcp_f32_e32 v229, v229
	v_rcp_f32_e32 v230, v230
	v_rcp_f32_e32 v231, v231
	v_rcp_f32_e32 v232, v232
	v_rcp_f32_e32 v233, v233
	v_rcp_f32_e32 v234, v234
	v_rcp_f32_e32 v235, v235
	v_pk_mul_f32 v[228:229], v[160:161], v[228:229]
	v_pk_mul_f32 v[230:231], v[162:163], v[230:231]
	v_pk_mul_f32 v[232:233], v[152:153], v[232:233]
	v_pk_mul_f32 v[234:235], v[154:155], v[234:235]
	v_pk_mul_f32 v[228:229], v[156:157], v[228:229]
	v_pk_mul_f32 v[230:231], v[158:159], v[230:231]
	v_pk_mul_f32 v[232:233], v[148:149], v[232:233]
	v_pk_mul_f32 v[234:235], v[150:151], v[234:235]
	v_cvt_pk_fp8_f32 v244, v228, v229
	v_cvt_pk_fp8_f32 v245, v232, v233
	v_cvt_pk_fp8_f32 v244, v230, v231 op_sel:[0,0,1]
	v_cvt_pk_fp8_f32 v245, v234, v235 op_sel:[0,0,1]
	s_nop 0
	global_store_dwordx2 v[8:9], v[244:245], off
	v_or_b32_e32 v4, 48, v4
	v_ashrrev_i32_e32 v5, 31, v4
	v_lshlrev_b64 v[4:5], 9, v[4:5]
	v_lshl_add_u64 v[4:5], s[24:25], 0, v[4:5]
	v_lshl_add_u64 v[2:3], v[4:5], 0, v[2:3]
	v_pk_mul_f32 v[228:229], v[144:145], s[98:99] op_sel_hi:[1,0]
	v_pk_mul_f32 v[230:231], v[146:147], s[98:99] op_sel_hi:[1,0]
	v_pk_mul_f32 v[232:233], v[136:137], s[98:99] op_sel_hi:[1,0]
; __device__ __forceinline__ unsigned pk4_fp8(float a, float b, float c, float d) { int r = __builtin_amdgcn_cvt_pk_fp8_f32(a, b, 0, false); r = __builtin_amdgcn_cvt_pk_fp8_f32(c, d, r, true); return (unsigned)r; }
;     __device__ __forceinline__ void operator()(const f32x4 (&acc)[2][2][4][2], const Unit& u, int wr, int wc, int fr, int fq) const {
;         const int row0 = u.pm * BM + wr * 64 + fr, col0 = (u.pn & 3) * 128 + wc * 32 + 8 * fq;
; #pragma unroll
;         for (int ai = 0; ai < 2; ++ai)
; #pragma unroll
;             for (int m = 0; m < 4; ++m) { float r[8];
; #pragma unroll
;                 for (int n = 0; n < 2; ++n)
; #pragma unroll
;                     for (int e = 0; e < 4; ++e) { const float g = acc[ai][0][m][n][e], up = acc[ai][1][m][n][e]; r[4 * n + e] = g * __builtin_amdgcn_rcpf(1.0f + __builtin_amdgcn_exp2f(-g * LOG2E)) * up * (float)(1 << ASHIFT); }
;                 v2u w; w.x = pk4_fp8(r[0], r[1], r[2], r[3]); w.y = pk4_fp8(r[4], r[5], r[6], r[7]);
;                 *(v2u*)(O + (size_t)(row0 + ai * HALF + m * 16) * EH + col0) = w; }
;     }
	v_pk_mul_f32 v[234:235], v[138:139], s[98:99] op_sel_hi:[1,0]
	v_exp_f32_e32 v228, v228
	v_exp_f32_e32 v229, v229
	v_exp_f32_e32 v230, v230
	v_exp_f32_e32 v231, v231
	v_exp_f32_e32 v232, v232
	v_exp_f32_e32 v233, v233
	v_exp_f32_e32 v234, v234
	v_exp_f32_e32 v235, v235
	v_pk_add_f32 v[228:229], v[228:229], 1.0 op_sel_hi:[1,0]
	v_pk_add_f32 v[230:231], v[230:231], 1.0 op_sel_hi:[1,0]
	v_pk_add_f32 v[232:233], v[232:233], 1.0 op_sel_hi:[1,0]
	v_pk_add_f32 v[234:235], v[234:235], 1.0 op_sel_hi:[1,0]
	v_rcp_f32_e32 v228, v228
	v_rcp_f32_e32 v229, v229
	v_rcp_f32_e32 v230, v230
	v_rcp_f32_e32 v231, v231
	v_rcp_f32_e32 v232, v232
	v_rcp_f32_e32 v233, v233
	v_rcp_f32_e32 v234, v234
	v_rcp_f32_e32 v235, v235
	v_pk_mul_f32 v[228:229], v[144:145], v[228:229]
	v_pk_mul_f32 v[230:231], v[146:147], v[230:231]
	v_pk_mul_f32 v[232:233], v[136:137], v[232:233]
	v_pk_mul_f32 v[234:235], v[138:139], v[234:235]
	v_pk_mul_f32 v[228:229], v[140:141], v[228:229]
	v_pk_mul_f32 v[230:231], v[142:143], v[230:231]
	v_pk_mul_f32 v[232:233], v[132:133], v[232:233]
	v_pk_mul_f32 v[234:235], v[134:135], v[234:235]
	v_cvt_pk_fp8_f32 v244, v228, v229
	v_cvt_pk_fp8_f32 v245, v232, v233
	v_cvt_pk_fp8_f32 v244, v230, v231 op_sel:[0,0,1]
	v_cvt_pk_fp8_f32 v245, v234, v235 op_sel:[0,0,1]
	s_nop 0
	global_store_dwordx2 v[2:3], v[244:245], off
	v_add_co_u32_e32 v4, vcc, s50, v0
	s_nop 0
	v_addc_co_u32_e32 v5, vcc, 0, v1, vcc
	v_pk_mul_f32 v[228:229], v[128:129], s[98:99] op_sel_hi:[1,0]
	v_pk_mul_f32 v[230:231], v[130:131], s[98:99] op_sel_hi:[1,0]
	v_pk_mul_f32 v[232:233], v[120:121], s[98:99] op_sel_hi:[1,0]
	v_pk_mul_f32 v[234:235], v[122:123], s[98:99] op_sel_hi:[1,0]
	v_exp_f32_e32 v228, v228
	v_exp_f32_e32 v229, v229
	v_exp_f32_e32 v230, v230
	v_exp_f32_e32 v231, v231
	v_exp_f32_e32 v232, v232
	v_exp_f32_e32 v233, v233
	v_exp_f32_e32 v234, v234
	v_exp_f32_e32 v235, v235
	v_pk_add_f32 v[228:229], v[228:229], 1.0 op_sel_hi:[1,0]
	v_pk_add_f32 v[230:231], v[230:231], 1.0 op_sel_hi:[1,0]
	v_pk_add_f32 v[232:233], v[232:233], 1.0 op_sel_hi:[1,0]
	v_pk_add_f32 v[234:235], v[234:235], 1.0 op_sel_hi:[1,0]
	v_rcp_f32_e32 v228, v228
	v_rcp_f32_e32 v229, v229
	v_rcp_f32_e32 v230, v230
	v_rcp_f32_e32 v231, v231
	v_rcp_f32_e32 v232, v232
	v_rcp_f32_e32 v233, v233
	v_rcp_f32_e32 v234, v234
	v_rcp_f32_e32 v235, v235
	v_pk_mul_f32 v[228:229], v[128:129], v[228:229]
	v_pk_mul_f32 v[230:231], v[130:131], v[230:231]
	v_pk_mul_f32 v[232:233], v[120:121], v[232:233]
	v_pk_mul_f32 v[234:235], v[122:123], v[234:235]
	v_pk_mul_f32 v[228:229], v[124:125], v[228:229]
	v_pk_mul_f32 v[230:231], v[126:127], v[230:231]
	v_pk_mul_f32 v[232:233], v[116:117], v[232:233]
	v_pk_mul_f32 v[234:235], v[118:119], v[234:235]
	v_cvt_pk_fp8_f32 v244, v228, v229
	v_cvt_pk_fp8_f32 v245, v232, v233
	v_cvt_pk_fp8_f32 v244, v230, v231 op_sel:[0,0,1]
	v_cvt_pk_fp8_f32 v245, v234, v235 op_sel:[0,0,1]
	s_nop 0
	global_store_dwordx2 v[4:5], v[244:245], off
	v_add_co_u32_e32 v4, vcc, s52, v0
	s_nop 0
	v_addc_co_u32_e32 v5, vcc, 0, v1, vcc
	v_pk_mul_f32 v[228:229], v[112:113], s[98:99] op_sel_hi:[1,0]
	v_pk_mul_f32 v[230:231], v[114:115], s[98:99] op_sel_hi:[1,0]
	v_pk_mul_f32 v[232:233], v[104:105], s[98:99] op_sel_hi:[1,0]
	v_pk_mul_f32 v[234:235], v[106:107], s[98:99] op_sel_hi:[1,0]
	v_exp_f32_e32 v228, v228
	v_exp_f32_e32 v229, v229
	v_exp_f32_e32 v230, v230
	v_exp_f32_e32 v231, v231
	v_exp_f32_e32 v232, v232
	v_exp_f32_e32 v233, v233
	v_exp_f32_e32 v234, v234
	v_exp_f32_e32 v235, v235
	v_pk_add_f32 v[228:229], v[228:229], 1.0 op_sel_hi:[1,0]
	v_pk_add_f32 v[230:231], v[230:231], 1.0 op_sel_hi:[1,0]
	v_pk_add_f32 v[232:233], v[232:233], 1.0 op_sel_hi:[1,0]
	v_pk_add_f32 v[234:235], v[234:235], 1.0 op_sel_hi:[1,0]
	v_rcp_f32_e32 v228, v228
	v_rcp_f32_e32 v229, v229
	v_rcp_f32_e32 v230, v230
	v_rcp_f32_e32 v231, v231
	v_rcp_f32_e32 v232, v232
	v_rcp_f32_e32 v233, v233
	v_rcp_f32_e32 v234, v234
	v_rcp_f32_e32 v235, v235
; #define PG8_BAR __builtin_amdgcn_s_barrier()
; __device__ __forceinline__ unsigned pk4_fp8(float a, float b, float c, float d) { int r = __builtin_amdgcn_cvt_pk_fp8_f32(a, b, 0, false); r = __builtin_amdgcn_cvt_pk_fp8_f32(c, d, r, true); return (unsigned)r; }
; template <class Epi, class Sched, bool ALIGN_EPI, bool FP8 = false>
; __device__ __forceinline__ void gemm_phase(PG8_LAS unsigned char* lds, const Gemm g, const Sched& S, const Epi& E, const int wid, const int lane) {
;     ...
;         if (!has_next) break;
; #pragma unroll
;         for (int a = 0; a < 2; ++a)
; #pragma unroll
;             for (int b = 0; b < 2; ++b)
; #pragma unroll
;                 for (int m = 0; m < 4; ++m)
; #pragma unroll
;                     for (int n = 0; n < 2; ++n) acc[a][b][m][n] = (f32x4){0.f, 0.f, 0.f, 0.f};
;         cur = nxt; cA = nA; cB = nB; ++ui;
;         if constexpr (ALIGN_EPI) { if (wr == 1) PG8_BAR; }
;     __device__ __forceinline__ void operator()(const f32x4 (&acc)[2][2][4][2], const Unit& u, int wr, int wc, int fr, int fq) const {
;         const int row0 = u.pm * BM + wr * 64 + fr, col0 = (u.pn & 3) * 128 + wc * 32 + 8 * fq;
; #pragma unroll
;         for (int ai = 0; ai < 2; ++ai)
; #pragma unroll
;             for (int m = 0; m < 4; ++m) { float r[8];
; #pragma unroll
;                 for (int n = 0; n < 2; ++n)
; #pragma unroll
;                     for (int e = 0; e < 4; ++e) { const float g = acc[ai][0][m][n][e], up = acc[ai][1][m][n][e]; r[4 * n + e] = g * __builtin_amdgcn_rcpf(1.0f + __builtin_amdgcn_exp2f(-g * LOG2E)) * up * (float)(1 << ASHIFT); }
;                 v2u w; w.x = pk4_fp8(r[0], r[1], r[2], r[3]); w.y = pk4_fp8(r[4], r[5], r[6], r[7]);
;                 *(v2u*)(O + (size_t)(row0 + ai * HALF + m * 16) * EH + col0) = w; }
;     }
	v_pk_mul_f32 v[228:229], v[112:113], v[228:229]
	v_pk_mul_f32 v[230:231], v[114:115], v[230:231]
	v_pk_mul_f32 v[232:233], v[104:105], v[232:233]
	v_pk_mul_f32 v[234:235], v[106:107], v[234:235]
	v_pk_mul_f32 v[228:229], v[108:109], v[228:229]
	v_pk_mul_f32 v[230:231], v[110:111], v[230:231]
	v_pk_mul_f32 v[232:233], v[100:101], v[232:233]
	v_pk_mul_f32 v[234:235], v[102:103], v[234:235]
	v_cvt_pk_fp8_f32 v244, v228, v229
	v_cvt_pk_fp8_f32 v245, v232, v233
	v_cvt_pk_fp8_f32 v244, v230, v231 op_sel:[0,0,1]
	v_cvt_pk_fp8_f32 v245, v234, v235 op_sel:[0,0,1]
	s_nop 0
	global_store_dwordx2 v[4:5], v[244:245], off
	v_add_co_u32_e32 v4, vcc, s54, v0
	s_nop 0
	v_addc_co_u32_e32 v5, vcc, 0, v1, vcc
	v_pk_mul_f32 v[228:229], v[96:97], s[98:99] op_sel_hi:[1,0]
	v_pk_mul_f32 v[230:231], v[98:99], s[98:99] op_sel_hi:[1,0]
	v_pk_mul_f32 v[232:233], v[88:89], s[98:99] op_sel_hi:[1,0]
	v_pk_mul_f32 v[234:235], v[90:91], s[98:99] op_sel_hi:[1,0]
	v_exp_f32_e32 v228, v228
	v_exp_f32_e32 v229, v229
	v_exp_f32_e32 v230, v230
	v_exp_f32_e32 v231, v231
	v_exp_f32_e32 v232, v232
	v_exp_f32_e32 v233, v233
	v_exp_f32_e32 v234, v234
	v_exp_f32_e32 v235, v235
	v_pk_add_f32 v[228:229], v[228:229], 1.0 op_sel_hi:[1,0]
	v_pk_add_f32 v[230:231], v[230:231], 1.0 op_sel_hi:[1,0]
	v_pk_add_f32 v[232:233], v[232:233], 1.0 op_sel_hi:[1,0]
	v_pk_add_f32 v[234:235], v[234:235], 1.0 op_sel_hi:[1,0]
	v_rcp_f32_e32 v228, v228
	v_rcp_f32_e32 v229, v229
	v_rcp_f32_e32 v230, v230
	v_rcp_f32_e32 v231, v231
	v_rcp_f32_e32 v232, v232
	v_rcp_f32_e32 v233, v233
	v_rcp_f32_e32 v234, v234
	v_rcp_f32_e32 v235, v235
	v_pk_mul_f32 v[228:229], v[96:97], v[228:229]
	v_pk_mul_f32 v[230:231], v[98:99], v[230:231]
	v_pk_mul_f32 v[232:233], v[88:89], v[232:233]
	v_pk_mul_f32 v[234:235], v[90:91], v[234:235]
	v_pk_mul_f32 v[228:229], v[92:93], v[228:229]
	v_pk_mul_f32 v[230:231], v[94:95], v[230:231]
	v_pk_mul_f32 v[232:233], v[84:85], v[232:233]
	v_pk_mul_f32 v[234:235], v[86:87], v[234:235]
	v_cvt_pk_fp8_f32 v244, v228, v229
	v_cvt_pk_fp8_f32 v245, v232, v233
	v_cvt_pk_fp8_f32 v244, v230, v231 op_sel:[0,0,1]
	v_cvt_pk_fp8_f32 v245, v234, v235 op_sel:[0,0,1]
	s_nop 0
	global_store_dwordx2 v[4:5], v[244:245], off
	v_add_co_u32_e32 v0, vcc, 0x16000, v0
	s_nop 1
	v_addc_co_u32_e32 v1, vcc, 0, v1, vcc
	s_and_b64 vcc, exec, s[4:5]
	s_mov_b64 s[4:5], -1
	v_pk_mul_f32 v[228:229], v[80:81], s[98:99] op_sel_hi:[1,0]
	v_pk_mul_f32 v[230:231], v[82:83], s[98:99] op_sel_hi:[1,0]
	v_pk_mul_f32 v[232:233], v[72:73], s[98:99] op_sel_hi:[1,0]
	v_pk_mul_f32 v[234:235], v[74:75], s[98:99] op_sel_hi:[1,0]
	v_exp_f32_e32 v228, v228
	v_exp_f32_e32 v229, v229
	v_exp_f32_e32 v230, v230
	v_exp_f32_e32 v231, v231
	v_exp_f32_e32 v232, v232
	v_exp_f32_e32 v233, v233
	v_exp_f32_e32 v234, v234
	v_exp_f32_e32 v235, v235
	v_pk_add_f32 v[228:229], v[228:229], 1.0 op_sel_hi:[1,0]
	v_pk_add_f32 v[230:231], v[230:231], 1.0 op_sel_hi:[1,0]
	v_pk_add_f32 v[232:233], v[232:233], 1.0 op_sel_hi:[1,0]
	v_pk_add_f32 v[234:235], v[234:235], 1.0 op_sel_hi:[1,0]
	v_rcp_f32_e32 v228, v228
	v_rcp_f32_e32 v229, v229
	v_rcp_f32_e32 v230, v230
	v_rcp_f32_e32 v231, v231
	v_rcp_f32_e32 v232, v232
	v_rcp_f32_e32 v233, v233
	v_rcp_f32_e32 v234, v234
	v_rcp_f32_e32 v235, v235
	v_pk_mul_f32 v[228:229], v[80:81], v[228:229]
	v_pk_mul_f32 v[230:231], v[82:83], v[230:231]
	v_pk_mul_f32 v[232:233], v[72:73], v[232:233]
	v_pk_mul_f32 v[234:235], v[74:75], v[234:235]
	v_pk_mul_f32 v[228:229], v[76:77], v[228:229]
	v_pk_mul_f32 v[230:231], v[78:79], v[230:231]
	v_pk_mul_f32 v[232:233], v[68:69], v[232:233]
	v_pk_mul_f32 v[234:235], v[70:71], v[234:235]
	v_cvt_pk_fp8_f32 v244, v228, v229
	v_cvt_pk_fp8_f32 v245, v232, v233
	v_cvt_pk_fp8_f32 v244, v230, v231 op_sel:[0,0,1]
	v_cvt_pk_fp8_f32 v245, v234, v235 op_sel:[0,0,1]
	s_nop 0
	global_store_dwordx2 v[0:1], v[244:245], off
	s_cbranch_vccnz .LBB0_1625
	s_andn2_b64 vcc, exec, s[22:23]
	s_cbranch_vccnz .LBB0_1624
	s_barrier
	s_branch .LBB0_1624
